# in-proj tile order r0 gelu|rope-q, r1 gelu-stat|sigmoid, r2 plain|rope-k, r3 sigmoid|sigmoid, r4 sigmoid (converters: rope, sigmoid, rope, sigmoid)
# baseline (speedup 1.0000x reference)
;     __device__ bool next(int i, Unit& u) const { if (!base.next(i >> 1, u)) return false; if (i & 1) { u.pm += MTOK / BM; u.pn += DM / BM; } return true; }
;   __device__ __forceinline__ bool next(int i,AttnUnit&u)const{ if(i>=2||vcu>=256)return false; const int s=vcu&3; u.bh=vcu>>2; u.qb=(i==0)?7-s:s; return true; }
;     __host__ __device__ bool next(int i, Unit& u) const {
;         const int L = i * G + c; if (L >= nwg) return false;
;         int wgid = L; { const int q = nwg / NXCD, r = nwg % NXCD, xcd = wgid % NXCD, off = wgid / NXCD; wgid = (xcd < r ? xcd * (q + 1) : r * (q + 1) + (xcd - r) * q) + off; }
;         const int nig = WGM * nN, gid = wgid / nig, fm = gid * WGM, gsz = (nM - fm) < WGM ? (nM - fm) : WGM;
;         u.pm = fm + ((wgid % nig) % gsz); u.pn = (wgid % nig) / gsz; u.half = 0; return true;
.LBB0_382:
	s_ashr_i32 s4, s21, 31
	s_lshr_b32 s4, s4, 29
	s_add_i32 s4, s21, s4
	s_ashr_i32 s5, s4, 3
	s_and_b32 s4, s4, -8
	s_sub_i32 s4, s21, s4
	s_cmp_lt_i32 s4, 0
	s_movk_i32 s6, 0x91
	s_cselect_b32 s6, s6, 0x90
	s_mul_i32 s4, s4, s6
	s_add_i32 s4, s4, s5
	s_mul_hi_i32 s5, s4, 0x38e38e39
	s_lshr_b32 s6, s5, 31
	s_ashr_i32 s5, s5, 5
	s_add_i32 s5, s5, s6
	s_lshl_b32 s6, s5, 3
	s_mulk_i32 s5, 0x90
	s_sub_i32 s4, s4, s5
	s_bfe_u32 s5, s4, 0x3001c
	s_add_i32 s5, s4, s5
	s_sext_i32_i16 s7, s5
	s_and_b32 s5, s5, 0xfff8
	s_sub_i32 s4, s4, s5
	s_sext_i32_i16 s4, s4
	s_add_i32 s18, s6, s4
	s_ashr_i32 s70, s7, 3
	s_mul_i32 s4, s70, 5
	s_cmp_lt_u32 s70, 12
	s_cbranch_scc0 .Lpn_hi0
	s_mov_b32 s6, 0x86229020
	s_mov_b32 s7, 0x399285a
	s_branch .Lpn_go0

;     __device__ bool next(int i, Unit& u) const { if (!base.next(i >> 1, u)) return false; if (i & 1) { u.pm += MTOK / BM; u.pn += DM / BM; } return true; }
;   __device__ __forceinline__ bool next(int i,AttnUnit&u)const{ if(i>=2||vcu>=256)return false; const int s=vcu&3; u.bh=vcu>>2; u.qb=(i==0)?7-s:s; return true; }
;     __host__ __device__ bool next(int i, Unit& u) const {
;         const int L = i * G + c; if (L >= nwg) return false;
;         int wgid = L; { const int q = nwg / NXCD, r = nwg % NXCD, xcd = wgid % NXCD, off = wgid / NXCD; wgid = (xcd < r ? xcd * (q + 1) : r * (q + 1) + (xcd - r) * q) + off; }
;         const int nig = WGM * nN, gid = wgid / nig, fm = gid * WGM, gsz = (nM - fm) < WGM ? (nM - fm) : WGM;
;         u.pm = fm + ((wgid % nig) % gsz); u.pn = (wgid % nig) / gsz; u.half = 0; return true;
; template <class Epi, class Sched, bool ALIGN_EPI = false, bool SP2 = false>
; __device__ __forceinline__ void gemm_phase(PG8_LAS unsigned char* lds, const Gemm g, const Sched& S, const Epi& E) {
;     ...
;         const bool has_next = S.next(ui + 1, nxt);
;         const char* nA = has_next ? (const char*)g.A + (size_t)nxt.pm * tstep + (nxt.half == 2 ? hstep : (size_t)0) : cA; const char* nB = has_next ? (const char*)g.Bt + (size_t)nxt.pn * tstep : cB;
.LBB0_392:
	s_add_i32 s72, s72, 1
	s_mul_i32 s10, s72, s33
	s_add_i32 s10, s10, s21
	s_cmpk_lt_i32 s10, 0x480
	s_cselect_b64 s[64:65], -1, 0
	s_cmpk_gt_i32 s10, 0x47f
	s_cbranch_scc1 .LBB0_394
	s_ashr_i32 s11, s10, 31
	s_lshr_b32 s11, s11, 29
	s_add_i32 s11, s10, s11
	s_ashr_i32 s12, s11, 3
	s_and_b32 s11, s11, -8
	s_sub_i32 s10, s10, s11
	s_cmp_lt_i32 s10, 0
	s_movk_i32 s11, 0x91
	s_cselect_b32 s11, s11, 0x90
	s_mul_i32 s10, s10, s11
	s_add_i32 s10, s10, s12
	s_mul_hi_i32 s11, s10, 0x38e38e39
	s_lshr_b32 s12, s11, 31
	s_ashr_i32 s11, s11, 5
	s_add_i32 s11, s11, s12
	s_lshl_b32 s12, s11, 3
	s_mulk_i32 s11, 0x90
	s_sub_i32 s10, s10, s11
	s_bfe_u32 s11, s10, 0x3001c
	s_add_i32 s11, s10, s11
	s_sext_i32_i16 s13, s11
	s_and_b32 s11, s11, 0xfff8
	s_sub_i32 s10, s10, s11
	s_sext_i32_i16 s10, s10
	s_add_i32 s60, s12, s10
	s_ashr_i32 s62, s13, 3
	s_mul_i32 s10, s62, 5
	s_cmp_lt_u32 s62, 12
	s_cbranch_scc0 .Lpn_hi1
	s_mov_b32 s12, 0x86229020
	s_mov_b32 s13, 0x399285a
	s_branch .Lpn_go1
